# v52 + accumulators zeroed with 64 v_mov_b64 (inline 0) instead of 128 dependent v_mov_b32 per unit in 8 GEMM loops
# speedup vs baseline: 1.0251x; 1.0047x over previous
.LBB0_176:
	s_add_u32 s56, s26, 0x100
	s_addc_u32 s57, s27, 0
	v_mov_b32_e32 v167, v165
	v_mov_b32_e32 v169, v165
	s_add_u32 s58, s28, 0x100
	v_mov_b64_e32 v[32:33], 0
	v_mov_b64_e32 v[34:35], 0
	v_mov_b64_e32 v[36:37], 0
	v_mov_b64_e32 v[38:39], 0
	v_mov_b64_e32 v[40:41], 0
	v_mov_b64_e32 v[42:43], 0
	v_mov_b64_e32 v[44:45], 0
	v_mov_b64_e32 v[46:47], 0
	v_mov_b64_e32 v[48:49], 0
	v_mov_b64_e32 v[50:51], 0
	v_mov_b64_e32 v[52:53], 0
	v_mov_b64_e32 v[54:55], 0
	v_mov_b64_e32 v[56:57], 0
	v_mov_b64_e32 v[58:59], 0
	v_mov_b64_e32 v[60:61], 0
	v_mov_b64_e32 v[62:63], 0
	v_mov_b64_e32 v[64:65], 0
	v_mov_b64_e32 v[66:67], 0
	v_mov_b64_e32 v[68:69], 0
	v_mov_b64_e32 v[70:71], 0
	v_mov_b64_e32 v[72:73], 0
	v_mov_b64_e32 v[74:75], 0
	v_mov_b64_e32 v[76:77], 0
	v_mov_b64_e32 v[78:79], 0
	v_mov_b64_e32 v[80:81], 0
	v_mov_b64_e32 v[82:83], 0
	v_mov_b64_e32 v[84:85], 0
	v_mov_b64_e32 v[86:87], 0
	v_mov_b64_e32 v[88:89], 0
	v_mov_b64_e32 v[90:91], 0
	v_mov_b64_e32 v[92:93], 0
	v_mov_b64_e32 v[94:95], 0
	v_mov_b64_e32 v[96:97], 0
	v_mov_b64_e32 v[98:99], 0
	v_mov_b64_e32 v[100:101], 0
	v_mov_b64_e32 v[102:103], 0
	v_mov_b64_e32 v[104:105], 0
	v_mov_b64_e32 v[106:107], 0
	v_mov_b64_e32 v[108:109], 0
	v_mov_b64_e32 v[110:111], 0
	v_mov_b64_e32 v[112:113], 0
	v_mov_b64_e32 v[114:115], 0
	v_mov_b64_e32 v[116:117], 0
	v_mov_b64_e32 v[118:119], 0
	v_mov_b64_e32 v[120:121], 0
	v_mov_b64_e32 v[122:123], 0
	v_mov_b64_e32 v[124:125], 0
	v_mov_b64_e32 v[126:127], 0
	v_mov_b64_e32 v[128:129], 0
	v_mov_b64_e32 v[130:131], 0
	v_mov_b64_e32 v[132:133], 0
	v_mov_b64_e32 v[134:135], 0
	v_mov_b64_e32 v[136:137], 0
	v_mov_b64_e32 v[138:139], 0
	v_mov_b64_e32 v[140:141], 0
	v_mov_b64_e32 v[142:143], 0
	v_mov_b64_e32 v[144:145], 0
	v_mov_b64_e32 v[146:147], 0
	v_mov_b64_e32 v[148:149], 0
	v_mov_b64_e32 v[150:151], 0
	v_mov_b64_e32 v[152:153], 0
	v_mov_b64_e32 v[154:155], 0
	v_mov_b64_e32 v[156:157], 0
	v_mov_b64_e32 v[158:159], 0
	v_mov_b32_e32 v175, v165
	v_mov_b32_e32 v177, v165
	v_lshl_add_u64 v[178:179], s[16:17], 0, v[168:169]
	v_lshl_add_u64 v[180:181], s[16:17], 0, v[166:167]
	s_addc_u32 s59, s29, 0
	s_mov_b32 s60, -2
	s_mov_b64 s[26:27], 0
	v_add_u32_e32 v252, 0x10000, v204
	v_add_u32_e32 v253, 0x10000, v205
	s_branch .LBB0_178

.LBB0_589:
	s_lshl_b32 s4, s80, 10
	s_and_b32 s4, s4, 0x400
	s_add_u32 s27, s38, 0x100
	s_addc_u32 s86, s39, 0
	v_mov_b32_e32 v171, v165
	v_mov_b32_e32 v169, v165
	s_add_u32 s87, s40, 0x100
	v_mov_b64_e32 v[32:33], 0
	v_mov_b64_e32 v[34:35], 0
	v_mov_b64_e32 v[36:37], 0
	v_mov_b64_e32 v[38:39], 0
	v_mov_b64_e32 v[40:41], 0
	v_mov_b64_e32 v[42:43], 0
	v_mov_b64_e32 v[44:45], 0
	v_mov_b64_e32 v[46:47], 0
	v_mov_b64_e32 v[48:49], 0
	v_mov_b64_e32 v[50:51], 0
	v_mov_b64_e32 v[52:53], 0
	v_mov_b64_e32 v[54:55], 0
	v_mov_b64_e32 v[56:57], 0
	v_mov_b64_e32 v[58:59], 0
	v_mov_b64_e32 v[60:61], 0
	v_mov_b64_e32 v[62:63], 0
	v_mov_b64_e32 v[64:65], 0
	v_mov_b64_e32 v[66:67], 0
	v_mov_b64_e32 v[68:69], 0
	v_mov_b64_e32 v[70:71], 0
	v_mov_b64_e32 v[72:73], 0
	v_mov_b64_e32 v[74:75], 0
	v_mov_b64_e32 v[76:77], 0
	v_mov_b64_e32 v[78:79], 0
	v_mov_b64_e32 v[80:81], 0
	v_mov_b64_e32 v[82:83], 0
	v_mov_b64_e32 v[84:85], 0
	v_mov_b64_e32 v[86:87], 0
	v_mov_b64_e32 v[88:89], 0
	v_mov_b64_e32 v[90:91], 0
	v_mov_b64_e32 v[92:93], 0
	v_mov_b64_e32 v[94:95], 0
	v_mov_b64_e32 v[96:97], 0
	v_mov_b64_e32 v[98:99], 0
	v_mov_b64_e32 v[100:101], 0
	v_mov_b64_e32 v[102:103], 0
	v_mov_b64_e32 v[104:105], 0
	v_mov_b64_e32 v[106:107], 0
	v_mov_b64_e32 v[108:109], 0
	v_mov_b64_e32 v[110:111], 0
	v_mov_b64_e32 v[112:113], 0
	v_mov_b64_e32 v[114:115], 0
	v_mov_b64_e32 v[116:117], 0
	v_mov_b64_e32 v[118:119], 0
	v_mov_b64_e32 v[120:121], 0
	v_mov_b64_e32 v[122:123], 0
	v_mov_b64_e32 v[124:125], 0
	v_mov_b64_e32 v[126:127], 0
	v_mov_b64_e32 v[128:129], 0
	v_mov_b64_e32 v[130:131], 0
	v_mov_b64_e32 v[132:133], 0
	v_mov_b64_e32 v[134:135], 0
	v_mov_b64_e32 v[136:137], 0
	v_mov_b64_e32 v[138:139], 0
	v_mov_b64_e32 v[140:141], 0
	v_mov_b64_e32 v[142:143], 0
	v_mov_b64_e32 v[144:145], 0
	v_mov_b64_e32 v[146:147], 0
	v_mov_b64_e32 v[148:149], 0
	v_mov_b64_e32 v[150:151], 0
	v_mov_b64_e32 v[152:153], 0
	v_mov_b64_e32 v[154:155], 0
	v_mov_b64_e32 v[156:157], 0
	v_mov_b64_e32 v[158:159], 0
	v_add_u32_e32 v208, s4, v199
	v_lshl_add_u64 v[174:175], s[18:19], 0, v[168:169]
	v_lshl_add_u64 v[176:177], s[18:19], 0, v[170:171]
	s_addc_u32 s88, s41, 0
	s_mov_b32 s89, -2
	s_mov_b64 s[4:5], 0
	v_add_u32_e32 v252, 0x10000, v197
	v_add_u32_e32 v253, 0x10000, v198
	s_branch .LBB0_591

.LBB0_671:
	s_add_u32 s27, s34, 0x100
	s_addc_u32 s82, s35, 0
	v_mov_b32_e32 v167, v165
	v_mov_b32_e32 v169, v165
	s_add_u32 s83, s38, 0x100
	v_mov_b64_e32 v[32:33], 0
	v_mov_b64_e32 v[34:35], 0
	v_mov_b64_e32 v[36:37], 0
	v_mov_b64_e32 v[38:39], 0
	v_mov_b64_e32 v[40:41], 0
	v_mov_b64_e32 v[42:43], 0
	v_mov_b64_e32 v[44:45], 0
	v_mov_b64_e32 v[46:47], 0
	v_mov_b64_e32 v[48:49], 0
	v_mov_b64_e32 v[50:51], 0
	v_mov_b64_e32 v[52:53], 0
	v_mov_b64_e32 v[54:55], 0
	v_mov_b64_e32 v[56:57], 0
	v_mov_b64_e32 v[58:59], 0
	v_mov_b64_e32 v[60:61], 0
	v_mov_b64_e32 v[62:63], 0
	v_mov_b64_e32 v[64:65], 0
	v_mov_b64_e32 v[66:67], 0
	v_mov_b64_e32 v[68:69], 0
	v_mov_b64_e32 v[70:71], 0
	v_mov_b64_e32 v[72:73], 0
	v_mov_b64_e32 v[74:75], 0
	v_mov_b64_e32 v[76:77], 0
	v_mov_b64_e32 v[78:79], 0
	v_mov_b64_e32 v[80:81], 0
	v_mov_b64_e32 v[82:83], 0
	v_mov_b64_e32 v[84:85], 0
	v_mov_b64_e32 v[86:87], 0
	v_mov_b64_e32 v[88:89], 0
	v_mov_b64_e32 v[90:91], 0
	v_mov_b64_e32 v[92:93], 0
	v_mov_b64_e32 v[94:95], 0
	v_mov_b64_e32 v[96:97], 0
	v_mov_b64_e32 v[98:99], 0
	v_mov_b64_e32 v[100:101], 0
	v_mov_b64_e32 v[102:103], 0
	v_mov_b64_e32 v[104:105], 0
	v_mov_b64_e32 v[106:107], 0
	v_mov_b64_e32 v[108:109], 0
	v_mov_b64_e32 v[110:111], 0
	v_mov_b64_e32 v[112:113], 0
	v_mov_b64_e32 v[114:115], 0
	v_mov_b64_e32 v[116:117], 0
	v_mov_b64_e32 v[118:119], 0
	v_mov_b64_e32 v[120:121], 0
	v_mov_b64_e32 v[122:123], 0
	v_mov_b64_e32 v[124:125], 0
	v_mov_b64_e32 v[126:127], 0
	v_mov_b64_e32 v[128:129], 0
	v_mov_b64_e32 v[130:131], 0
	v_mov_b64_e32 v[132:133], 0
	v_mov_b64_e32 v[134:135], 0
	v_mov_b64_e32 v[136:137], 0
	v_mov_b64_e32 v[138:139], 0
	v_mov_b64_e32 v[140:141], 0
	v_mov_b64_e32 v[142:143], 0
	v_mov_b64_e32 v[144:145], 0
	v_mov_b64_e32 v[146:147], 0
	v_mov_b64_e32 v[148:149], 0
	v_mov_b64_e32 v[150:151], 0
	v_mov_b64_e32 v[152:153], 0
	v_mov_b64_e32 v[154:155], 0
	v_mov_b64_e32 v[156:157], 0
	v_mov_b64_e32 v[158:159], 0
	v_mov_b32_e32 v175, v165
	v_mov_b32_e32 v177, v165
	v_lshl_add_u64 v[178:179], s[16:17], 0, v[168:169]
	v_lshl_add_u64 v[180:181], s[16:17], 0, v[166:167]
	s_addc_u32 s84, s39, 0
	s_mov_b32 s85, -2
	s_mov_b64 s[34:35], 0
	v_add_u32_e32 v252, 0x10000, v205
	v_add_u32_e32 v253, 0x10000, v206
	s_branch .LBB0_673

.LBB0_816:
	s_add_u32 s56, s26, 0x100
	s_addc_u32 s57, s27, 0
	v_mov_b32_e32 v169, v165
	v_mov_b32_e32 v171, v165
	s_add_u32 s58, s28, 0x100
	v_mov_b64_e32 v[32:33], 0
	v_mov_b64_e32 v[34:35], 0
	v_mov_b64_e32 v[36:37], 0
	v_mov_b64_e32 v[38:39], 0
	v_mov_b64_e32 v[40:41], 0
	v_mov_b64_e32 v[42:43], 0
	v_mov_b64_e32 v[44:45], 0
	v_mov_b64_e32 v[46:47], 0
	v_mov_b64_e32 v[48:49], 0
	v_mov_b64_e32 v[50:51], 0
	v_mov_b64_e32 v[52:53], 0
	v_mov_b64_e32 v[54:55], 0
	v_mov_b64_e32 v[56:57], 0
	v_mov_b64_e32 v[58:59], 0
	v_mov_b64_e32 v[60:61], 0
	v_mov_b64_e32 v[62:63], 0
	v_mov_b64_e32 v[64:65], 0
	v_mov_b64_e32 v[66:67], 0
	v_mov_b64_e32 v[68:69], 0
	v_mov_b64_e32 v[70:71], 0
	v_mov_b64_e32 v[72:73], 0
	v_mov_b64_e32 v[74:75], 0
	v_mov_b64_e32 v[76:77], 0
	v_mov_b64_e32 v[78:79], 0
	v_mov_b64_e32 v[80:81], 0
	v_mov_b64_e32 v[82:83], 0
	v_mov_b64_e32 v[84:85], 0
	v_mov_b64_e32 v[86:87], 0
	v_mov_b64_e32 v[88:89], 0
	v_mov_b64_e32 v[90:91], 0
	v_mov_b64_e32 v[92:93], 0
	v_mov_b64_e32 v[94:95], 0
	v_mov_b64_e32 v[96:97], 0
	v_mov_b64_e32 v[98:99], 0
	v_mov_b64_e32 v[100:101], 0
	v_mov_b64_e32 v[102:103], 0
	v_mov_b64_e32 v[104:105], 0
	v_mov_b64_e32 v[106:107], 0
	v_mov_b64_e32 v[108:109], 0
	v_mov_b64_e32 v[110:111], 0
	v_mov_b64_e32 v[112:113], 0
	v_mov_b64_e32 v[114:115], 0
	v_mov_b64_e32 v[116:117], 0
	v_mov_b64_e32 v[118:119], 0
	v_mov_b64_e32 v[120:121], 0
	v_mov_b64_e32 v[122:123], 0
	v_mov_b64_e32 v[124:125], 0
	v_mov_b64_e32 v[126:127], 0
	v_mov_b64_e32 v[128:129], 0
	v_mov_b64_e32 v[130:131], 0
	v_mov_b64_e32 v[132:133], 0
	v_mov_b64_e32 v[134:135], 0
	v_mov_b64_e32 v[136:137], 0
	v_mov_b64_e32 v[138:139], 0
	v_mov_b64_e32 v[140:141], 0
	v_mov_b64_e32 v[142:143], 0
	v_mov_b64_e32 v[144:145], 0
	v_mov_b64_e32 v[146:147], 0
	v_mov_b64_e32 v[148:149], 0
	v_mov_b64_e32 v[150:151], 0
	v_mov_b64_e32 v[152:153], 0
	v_mov_b64_e32 v[154:155], 0
	v_mov_b64_e32 v[156:157], 0
	v_mov_b64_e32 v[158:159], 0
	v_mov_b32_e32 v175, v165
	v_mov_b32_e32 v177, v165
	v_lshl_add_u64 v[178:179], s[14:15], 0, v[170:171]
	v_lshl_add_u64 v[180:181], s[14:15], 0, v[168:169]
	s_addc_u32 s59, s29, 0
	s_mov_b32 s60, -2
	s_mov_b64 s[26:27], 0
	v_add_u32_e32 v252, 0x10000, v173
	v_add_u32_e32 v253, 0x10000, v206
	s_branch .LBB0_818

.LBB0_838:
	s_add_u32 s36, s4, 0x100
	s_addc_u32 s37, s5, 0
	v_mov_b32_e32 v129, v137
	v_mov_b32_e32 v131, v137
	s_add_u32 s57, s6, 0x100
	v_mov_b64_e32 v[0:1], 0
	v_mov_b64_e32 v[2:3], 0
	v_mov_b64_e32 v[4:5], 0
	v_mov_b64_e32 v[6:7], 0
	v_mov_b64_e32 v[8:9], 0
	v_mov_b64_e32 v[10:11], 0
	v_mov_b64_e32 v[12:13], 0
	v_mov_b64_e32 v[14:15], 0
	v_mov_b64_e32 v[16:17], 0
	v_mov_b64_e32 v[18:19], 0
	v_mov_b64_e32 v[20:21], 0
	v_mov_b64_e32 v[22:23], 0
	v_mov_b64_e32 v[24:25], 0
	v_mov_b64_e32 v[26:27], 0
	v_mov_b64_e32 v[28:29], 0
	v_mov_b64_e32 v[30:31], 0
	v_mov_b64_e32 v[32:33], 0
	v_mov_b64_e32 v[34:35], 0
	v_mov_b64_e32 v[36:37], 0
	v_mov_b64_e32 v[38:39], 0
	v_mov_b64_e32 v[40:41], 0
	v_mov_b64_e32 v[42:43], 0
	v_mov_b64_e32 v[44:45], 0
	v_mov_b64_e32 v[46:47], 0
	v_mov_b64_e32 v[48:49], 0
	v_mov_b64_e32 v[50:51], 0
	v_mov_b64_e32 v[52:53], 0
	v_mov_b64_e32 v[54:55], 0
	v_mov_b64_e32 v[56:57], 0
	v_mov_b64_e32 v[58:59], 0
	v_mov_b64_e32 v[60:61], 0
	v_mov_b64_e32 v[62:63], 0
	v_mov_b64_e32 v[64:65], 0
	v_mov_b64_e32 v[66:67], 0
	v_mov_b64_e32 v[68:69], 0
	v_mov_b64_e32 v[70:71], 0
	v_mov_b64_e32 v[72:73], 0
	v_mov_b64_e32 v[74:75], 0
	v_mov_b64_e32 v[76:77], 0
	v_mov_b64_e32 v[78:79], 0
	v_mov_b64_e32 v[80:81], 0
	v_mov_b64_e32 v[82:83], 0
	v_mov_b64_e32 v[84:85], 0
	v_mov_b64_e32 v[86:87], 0
	v_mov_b64_e32 v[88:89], 0
	v_mov_b64_e32 v[90:91], 0
	v_mov_b64_e32 v[92:93], 0
	v_mov_b64_e32 v[94:95], 0
	v_mov_b64_e32 v[96:97], 0
	v_mov_b64_e32 v[98:99], 0
	v_mov_b64_e32 v[100:101], 0
	v_mov_b64_e32 v[102:103], 0
	v_mov_b64_e32 v[104:105], 0
	v_mov_b64_e32 v[106:107], 0
	v_mov_b64_e32 v[108:109], 0
	v_mov_b64_e32 v[110:111], 0
	v_mov_b64_e32 v[112:113], 0
	v_mov_b64_e32 v[114:115], 0
	v_mov_b64_e32 v[116:117], 0
	v_mov_b64_e32 v[118:119], 0
	v_mov_b64_e32 v[120:121], 0
	v_mov_b64_e32 v[122:123], 0
	v_mov_b64_e32 v[124:125], 0
	v_mov_b64_e32 v[126:127], 0
	v_mov_b32_e32 v143, v137
	v_mov_b32_e32 v145, v137
	v_lshl_add_u64 v[146:147], s[22:23], 0, v[130:131]
	v_lshl_add_u64 v[148:149], s[22:23], 0, v[128:129]
	s_addc_u32 s60, s7, 0
	s_mov_b32 s61, -2
	s_mov_b64 s[4:5], 0
	v_add_u32_e32 v252, 0x10000, v159
	v_add_u32_e32 v253, 0x10000, v160
	s_branch .LBB0_840

.LBB0_1548:
	s_add_u32 s58, s24, 0x100
	s_addc_u32 s59, s25, 0
	v_mov_b32_e32 v169, v165
	v_mov_b32_e32 v171, v165
	s_add_u32 s60, s26, 0x100
	v_mov_b64_e32 v[32:33], 0
	v_mov_b64_e32 v[34:35], 0
	v_mov_b64_e32 v[36:37], 0
	v_mov_b64_e32 v[38:39], 0
	v_mov_b64_e32 v[40:41], 0
	v_mov_b64_e32 v[42:43], 0
	v_mov_b64_e32 v[44:45], 0
	v_mov_b64_e32 v[46:47], 0
	v_mov_b64_e32 v[48:49], 0
	v_mov_b64_e32 v[50:51], 0
	v_mov_b64_e32 v[52:53], 0
	v_mov_b64_e32 v[54:55], 0
	v_mov_b64_e32 v[56:57], 0
	v_mov_b64_e32 v[58:59], 0
	v_mov_b64_e32 v[60:61], 0
	v_mov_b64_e32 v[62:63], 0
	v_mov_b64_e32 v[64:65], 0
	v_mov_b64_e32 v[66:67], 0
	v_mov_b64_e32 v[68:69], 0
	v_mov_b64_e32 v[70:71], 0
	v_mov_b64_e32 v[72:73], 0
	v_mov_b64_e32 v[74:75], 0
	v_mov_b64_e32 v[76:77], 0
	v_mov_b64_e32 v[78:79], 0
	v_mov_b64_e32 v[80:81], 0
	v_mov_b64_e32 v[82:83], 0
	v_mov_b64_e32 v[84:85], 0
	v_mov_b64_e32 v[86:87], 0
	v_mov_b64_e32 v[88:89], 0
	v_mov_b64_e32 v[90:91], 0
	v_mov_b64_e32 v[92:93], 0
	v_mov_b64_e32 v[94:95], 0
	v_mov_b64_e32 v[96:97], 0
	v_mov_b64_e32 v[98:99], 0
	v_mov_b64_e32 v[100:101], 0
	v_mov_b64_e32 v[102:103], 0
	v_mov_b64_e32 v[104:105], 0
	v_mov_b64_e32 v[106:107], 0
	v_mov_b64_e32 v[108:109], 0
	v_mov_b64_e32 v[110:111], 0
	v_mov_b64_e32 v[112:113], 0
	v_mov_b64_e32 v[114:115], 0
	v_mov_b64_e32 v[116:117], 0
	v_mov_b64_e32 v[118:119], 0
	v_mov_b64_e32 v[120:121], 0
	v_mov_b64_e32 v[122:123], 0
	v_mov_b64_e32 v[124:125], 0
	v_mov_b64_e32 v[126:127], 0
	v_mov_b64_e32 v[128:129], 0
	v_mov_b64_e32 v[130:131], 0
	v_mov_b64_e32 v[132:133], 0
	v_mov_b64_e32 v[134:135], 0
	v_mov_b64_e32 v[136:137], 0
	v_mov_b64_e32 v[138:139], 0
	v_mov_b64_e32 v[140:141], 0
	v_mov_b64_e32 v[142:143], 0
	v_mov_b64_e32 v[144:145], 0
	v_mov_b64_e32 v[146:147], 0
	v_mov_b64_e32 v[148:149], 0
	v_mov_b64_e32 v[150:151], 0
	v_mov_b64_e32 v[152:153], 0
	v_mov_b64_e32 v[154:155], 0
	v_mov_b64_e32 v[156:157], 0
	v_mov_b64_e32 v[158:159], 0
	v_mov_b32_e32 v175, v165
	v_mov_b32_e32 v177, v165
	v_lshl_add_u64 v[178:179], s[14:15], 0, v[170:171]
	v_lshl_add_u64 v[180:181], s[14:15], 0, v[168:169]
	s_addc_u32 s61, s27, 0
	s_mov_b32 s62, -2
	s_mov_b64 s[24:25], 0
	s_waitcnt vmcnt(0)
	v_add_u32_e32 v252, 0x10000, v204
	v_add_u32_e32 v253, 0x10000, v205
	s_branch .LBB0_1550
